# code placement: s20 with the four GEMM K-loops' first byte at 0 mod 64 (unexecuted s_nop padding behind the preceding unconditional branch)
# baseline (speedup 1.0000x reference)
; #define PG8_STAGE(bufoff, gbase, voff) do { _Pragma("unroll") for (int _i = 0; _i < 2; ++_i) \
;         __builtin_amdgcn_global_load_lds((const unsigned*)((const char*)(gbase) + (voff)[_i]), (LAS unsigned*)(lds + (bufoff) + ldsw + _i * 8192), 16, 0, 0); } while (0)
; #define PG8_WAIT_V(n) asm volatile("s_waitcnt vmcnt(" #n ")" ::: "memory")
; #define PG8_BAR __builtin_amdgcn_s_barrier()
;     ...
;     Unit cur, nxt; int ui = 0;
;     if (!S.next(0, cur)) return;
;     f32x4 acc[2][2][4][2];
; #pragma unroll
;     for (int a = 0; a < 2; ++a)
; #pragma unroll
;         for (int b = 0; b < 2; ++b)
; #pragma unroll
;             for (int m = 0; m < 4; ++m)
; #pragma unroll
;                 for (int n = 0; n < 2; ++n) acc[a][b][m][n] = (f32x4){0.f, 0.f, 0.f, 0.f};
;     bf16x8 At[4][2], B0[2][2], B1[2][2];
;     unsigned va[2][2], vn[2][2];
;     PG8_ROWS(va, cur);
;     const char* cA = (const char*)A; const char* cB = S.b_base(cur);
;     PG8_WAIT_V(0);
;     PG8_STAGE(PG8_SB(0, 0), cB, voffB); PG8_STAGE(PG8_SB(0, 1), cB + hstep, voffB); PG8_STAGE(PG8_SA(0, 0), cA, va[0]); PG8_STAGE(PG8_SA(0, 1), cA, va[1]);
;     if (wr == 1) PG8_BAR;
;     PG8_WAIT_V(2); PG8_BAR;
;     PG8_STAGE(PG8_SB(1, 0), cB + kstep, voffB); PG8_STAGE(PG8_SA(1, 0), cA + kstep, va[0]); PG8_STAGE(PG8_SB(1, 1), cB + hstep + kstep, voffB);
;     PG8_WAIT_V(6); PG8_BAR;
;     for (;;) {
;         const bool has_next = S.next(ui + 1, nxt);
;         if (has_next) { PG8_ROWS(vn, nxt); }
;         else {
; #pragma unroll
;             for (int h = 0; h < 2; ++h)
; #pragma unroll
;                 for (int i = 0; i < 2; ++i) vn[h][i] = va[h][i]; }
;         const char* nB = has_next ? S.b_base(nxt) : cB;
;         for (int t = 0; t < nt; t += 2) {
;             const bool last = (t == nt - 2);
;             const char* a1 = cA + (size_t)(t + 1) * kstep;
;             const char* a2 = last ? cA : cA + (size_t)(t + 2) * kstep; const char* b2 = last ? nB : cB + (size_t)(t + 2) * kstep;
;             const char* a3 = a2 + kstep; const char* b3 = b2 + kstep;
;     ...
; #pragma unroll
;         for (int a = 0; a < 2; ++a)
; #pragma unroll
;             for (int b = 0; b < 2; ++b)
; #pragma unroll
;                 for (int m = 0; m < 4; ++m)
; #pragma unroll
;                     for (int n = 0; n < 2; ++n) acc[a][b][m][n] = (f32x4){0.f, 0.f, 0.f, 0.f};
;         cur = nxt; cB = nB; ++ui;
.LBB0_231:
	s_ashr_i32 s37, s36, 31
	s_lshl_b64 s[38:39], s[36:37], 20
	s_add_u32 s38, s3, s38
	s_addc_u32 s39, s21, s39
	s_and_b64 s[42:43], s[42:43], exec
	s_cselect_b32 s9, s39, s41
	s_cselect_b32 s37, s38, s40
	s_add_u32 s92, s40, 0x100
	v_mov_b32_e32 v2, 0
	v_mov_b32_e32 v209, v201
	v_mov_b32_e32 v211, v201
	s_addc_u32 s93, s41, 0
	s_mov_b32 s94, -2
	s_mov_b64 s[40:41], s[16:17]
	v_mov_b32_e32 v3, v2
	v_mov_b32_e32 v4, v2
	v_mov_b32_e32 v5, v2
	v_mov_b32_e32 v6, v2
	v_mov_b32_e32 v7, v2
	v_mov_b32_e32 v8, v2
	v_mov_b32_e32 v9, v2
	v_mov_b32_e32 v18, v2
	v_mov_b32_e32 v19, v2
	v_mov_b32_e32 v20, v2
	v_mov_b32_e32 v21, v2
	v_mov_b32_e32 v22, v2
	v_mov_b32_e32 v23, v2
	v_mov_b32_e32 v24, v2
	v_mov_b32_e32 v25, v2
	v_mov_b32_e32 v34, v2
	v_mov_b32_e32 v35, v2
	v_mov_b32_e32 v36, v2
	v_mov_b32_e32 v37, v2
	v_mov_b32_e32 v38, v2
	v_mov_b32_e32 v39, v2
	v_mov_b32_e32 v40, v2
	v_mov_b32_e32 v41, v2
	v_mov_b32_e32 v50, v2
	v_mov_b32_e32 v51, v2
	v_mov_b32_e32 v52, v2
	v_mov_b32_e32 v53, v2
	v_mov_b32_e32 v54, v2
	v_mov_b32_e32 v55, v2
	v_mov_b32_e32 v56, v2
	v_mov_b32_e32 v57, v2
	v_mov_b32_e32 v10, v2
	v_mov_b32_e32 v11, v2
	v_mov_b32_e32 v12, v2
	v_mov_b32_e32 v13, v2
	v_mov_b32_e32 v14, v2
	v_mov_b32_e32 v15, v2
	v_mov_b32_e32 v16, v2
	v_mov_b32_e32 v17, v2
	v_mov_b32_e32 v26, v2
	v_mov_b32_e32 v27, v2
	v_mov_b32_e32 v28, v2
	v_mov_b32_e32 v29, v2
	v_mov_b32_e32 v30, v2
	v_mov_b32_e32 v31, v2
	v_mov_b32_e32 v32, v2
	v_mov_b32_e32 v33, v2
	v_mov_b32_e32 v42, v2
	v_mov_b32_e32 v43, v2
	v_mov_b32_e32 v44, v2
	v_mov_b32_e32 v45, v2
	v_mov_b32_e32 v46, v2
	v_mov_b32_e32 v47, v2
	v_mov_b32_e32 v48, v2
	v_mov_b32_e32 v49, v2
	v_mov_b32_e32 v58, v2
	v_mov_b32_e32 v59, v2
	v_mov_b32_e32 v60, v2
	v_mov_b32_e32 v61, v2
	v_mov_b32_e32 v62, v2
	v_mov_b32_e32 v63, v2
	v_mov_b32_e32 v64, v2
	v_mov_b32_e32 v65, v2
	v_mov_b32_e32 v66, v2
	v_mov_b32_e32 v67, v2
	v_mov_b32_e32 v68, v2
	v_mov_b32_e32 v69, v2
	v_mov_b32_e32 v70, v2
	v_mov_b32_e32 v71, v2
	v_mov_b32_e32 v72, v2
	v_mov_b32_e32 v73, v2
	v_mov_b32_e32 v82, v2
	v_mov_b32_e32 v83, v2
	v_mov_b32_e32 v84, v2
	v_mov_b32_e32 v85, v2
	v_mov_b32_e32 v86, v2
	v_mov_b32_e32 v87, v2
	v_mov_b32_e32 v88, v2
	v_mov_b32_e32 v89, v2
	v_mov_b32_e32 v98, v2
	v_mov_b32_e32 v99, v2
	v_mov_b32_e32 v100, v2
	v_mov_b32_e32 v101, v2
	v_mov_b32_e32 v102, v2
	v_mov_b32_e32 v103, v2
	v_mov_b32_e32 v104, v2
	v_mov_b32_e32 v105, v2
	v_mov_b32_e32 v114, v2
	v_mov_b32_e32 v115, v2
	v_mov_b32_e32 v116, v2
	v_mov_b32_e32 v117, v2
	v_mov_b32_e32 v118, v2
	v_mov_b32_e32 v119, v2
	v_mov_b32_e32 v120, v2
	v_mov_b32_e32 v121, v2
	v_mov_b32_e32 v74, v2
	v_mov_b32_e32 v75, v2
	v_mov_b32_e32 v76, v2
	v_mov_b32_e32 v77, v2
	v_mov_b32_e32 v78, v2
	v_mov_b32_e32 v79, v2
	v_mov_b32_e32 v80, v2
	v_mov_b32_e32 v81, v2
	v_mov_b32_e32 v90, v2
	v_mov_b32_e32 v91, v2
	v_mov_b32_e32 v92, v2
	v_mov_b32_e32 v93, v2
	v_mov_b32_e32 v94, v2
	v_mov_b32_e32 v95, v2
	v_mov_b32_e32 v96, v2
	v_mov_b32_e32 v97, v2
	v_mov_b32_e32 v106, v2
	v_mov_b32_e32 v107, v2
	v_mov_b32_e32 v108, v2
	v_mov_b32_e32 v109, v2
	v_mov_b32_e32 v110, v2
	v_mov_b32_e32 v111, v2
	v_mov_b32_e32 v112, v2
	v_mov_b32_e32 v113, v2
	v_mov_b32_e32 v122, v2
	v_mov_b32_e32 v123, v2
	v_mov_b32_e32 v124, v2
	v_mov_b32_e32 v125, v2
	v_mov_b32_e32 v126, v2
	v_mov_b32_e32 v127, v2
	v_mov_b32_e32 v128, v2
	v_mov_b32_e32 v129, v2
	s_branch .LBB0_234
	s_nop 0
	s_nop 0
	s_nop 0
	s_nop 0
	s_nop 0
	s_nop 0
	s_nop 0
	s_nop 0
	s_nop 0

; #define PG8_STAGE(bufoff, gbase, voff) do { _Pragma("unroll") for (int _i = 0; _i < 2; ++_i) \
;         __builtin_amdgcn_global_load_lds((const unsigned*)((const char*)(gbase) + (voff)[_i]), (LAS unsigned*)(lds + (bufoff) + ldsw + _i * 8192), 16, 0, 0); } while (0)
; #define PG8_WAIT_V(n) asm volatile("s_waitcnt vmcnt(" #n ")" ::: "memory")
; #define PG8_BAR __builtin_amdgcn_s_barrier()
;     ...
;     Unit cur, nxt; int ui = 0;
;     if (!S.next(0, cur)) return;
;     f32x4 acc[2][2][4][2];
; #pragma unroll
;     for (int a = 0; a < 2; ++a)
; #pragma unroll
;         for (int b = 0; b < 2; ++b)
; #pragma unroll
;             for (int m = 0; m < 4; ++m)
; #pragma unroll
;                 for (int n = 0; n < 2; ++n) acc[a][b][m][n] = (f32x4){0.f, 0.f, 0.f, 0.f};
;     bf16x8 At[4][2], B0[2][2], B1[2][2];
;     unsigned va[2][2], vn[2][2];
;     PG8_ROWS(va, cur);
;     const char* cA = (const char*)A; const char* cB = S.b_base(cur);
;     PG8_WAIT_V(0);
;     PG8_STAGE(PG8_SB(0, 0), cB, voffB); PG8_STAGE(PG8_SB(0, 1), cB + hstep, voffB); PG8_STAGE(PG8_SA(0, 0), cA, va[0]); PG8_STAGE(PG8_SA(0, 1), cA, va[1]);
;     if (wr == 1) PG8_BAR;
;     PG8_WAIT_V(2); PG8_BAR;
;     PG8_STAGE(PG8_SB(1, 0), cB + kstep, voffB); PG8_STAGE(PG8_SA(1, 0), cA + kstep, va[0]); PG8_STAGE(PG8_SB(1, 1), cB + hstep + kstep, voffB);
;     PG8_WAIT_V(6); PG8_BAR;
;     for (;;) {
;         const bool has_next = S.next(ui + 1, nxt);
;         if (has_next) { PG8_ROWS(vn, nxt); }
;         else {
; #pragma unroll
;             for (int h = 0; h < 2; ++h)
; #pragma unroll
;                 for (int i = 0; i < 2; ++i) vn[h][i] = va[h][i]; }
;         const char* nB = has_next ? S.b_base(nxt) : cB;
;         for (int t = 0; t < nt; t += 2) {
;             const bool last = (t == nt - 2);
;             const char* a1 = cA + (size_t)(t + 1) * kstep;
;             const char* a2 = last ? cA : cA + (size_t)(t + 2) * kstep; const char* b2 = last ? nB : cB + (size_t)(t + 2) * kstep;
;             const char* a3 = a2 + kstep; const char* b3 = b2 + kstep;
;     ...
; #pragma unroll
;         for (int a = 0; a < 2; ++a)
; #pragma unroll
;             for (int b = 0; b < 2; ++b)
; #pragma unroll
;                 for (int m = 0; m < 4; ++m)
; #pragma unroll
;                     for (int n = 0; n < 2; ++n) acc[a][b][m][n] = (f32x4){0.f, 0.f, 0.f, 0.f};
;         cur = nxt; cB = nB; ++ui;
.LBB0_680:
	s_ashr_i32 s29, s28, 31
	s_lshl_b64 s[30:31], s[28:29], 20
	s_add_u32 s30, s27, s30
	s_addc_u32 s31, s33, s31
	s_and_b64 s[8:9], s[8:9], exec
	s_cselect_b32 s29, s31, s35
	s_cselect_b32 s56, s30, s34
	s_add_u32 s57, s34, 0x100
	v_mov_b32_e32 v2, 0
	v_mov_b32_e32 v213, v201
	v_mov_b32_e32 v215, v201
	s_addc_u32 s62, s35, 0
	s_mov_b32 s63, -2
	s_mov_b64 s[8:9], s[22:23]
	v_mov_b32_e32 v3, v2
	v_mov_b32_e32 v4, v2
	v_mov_b32_e32 v5, v2
	v_mov_b32_e32 v6, v2
	v_mov_b32_e32 v7, v2
	v_mov_b32_e32 v8, v2
	v_mov_b32_e32 v9, v2
	v_mov_b32_e32 v18, v2
	v_mov_b32_e32 v19, v2
	v_mov_b32_e32 v20, v2
	v_mov_b32_e32 v21, v2
	v_mov_b32_e32 v22, v2
	v_mov_b32_e32 v23, v2
	v_mov_b32_e32 v24, v2
	v_mov_b32_e32 v25, v2
	v_mov_b32_e32 v34, v2
	v_mov_b32_e32 v35, v2
	v_mov_b32_e32 v36, v2
	v_mov_b32_e32 v37, v2
	v_mov_b32_e32 v38, v2
	v_mov_b32_e32 v39, v2
	v_mov_b32_e32 v40, v2
	v_mov_b32_e32 v41, v2
	v_mov_b32_e32 v50, v2
	v_mov_b32_e32 v51, v2
	v_mov_b32_e32 v52, v2
	v_mov_b32_e32 v53, v2
	v_mov_b32_e32 v54, v2
	v_mov_b32_e32 v55, v2
	v_mov_b32_e32 v56, v2
	v_mov_b32_e32 v57, v2
	v_mov_b32_e32 v10, v2
	v_mov_b32_e32 v11, v2
	v_mov_b32_e32 v12, v2
	v_mov_b32_e32 v13, v2
	v_mov_b32_e32 v14, v2
	v_mov_b32_e32 v15, v2
	v_mov_b32_e32 v16, v2
	v_mov_b32_e32 v17, v2
	v_mov_b32_e32 v26, v2
	v_mov_b32_e32 v27, v2
	v_mov_b32_e32 v28, v2
	v_mov_b32_e32 v29, v2
	v_mov_b32_e32 v30, v2
	v_mov_b32_e32 v31, v2
	v_mov_b32_e32 v32, v2
	v_mov_b32_e32 v33, v2
	v_mov_b32_e32 v42, v2
	v_mov_b32_e32 v43, v2
	v_mov_b32_e32 v44, v2
	v_mov_b32_e32 v45, v2
	v_mov_b32_e32 v46, v2
	v_mov_b32_e32 v47, v2
	v_mov_b32_e32 v48, v2
	v_mov_b32_e32 v49, v2
	v_mov_b32_e32 v58, v2
	v_mov_b32_e32 v59, v2
	v_mov_b32_e32 v60, v2
	v_mov_b32_e32 v61, v2
	v_mov_b32_e32 v62, v2
	v_mov_b32_e32 v63, v2
	v_mov_b32_e32 v64, v2
	v_mov_b32_e32 v65, v2
	v_mov_b32_e32 v66, v2
	v_mov_b32_e32 v67, v2
	v_mov_b32_e32 v68, v2
	v_mov_b32_e32 v69, v2
	v_mov_b32_e32 v70, v2
	v_mov_b32_e32 v71, v2
	v_mov_b32_e32 v72, v2
	v_mov_b32_e32 v73, v2
	v_mov_b32_e32 v82, v2
	v_mov_b32_e32 v83, v2
	v_mov_b32_e32 v84, v2
	v_mov_b32_e32 v85, v2
	v_mov_b32_e32 v86, v2
	v_mov_b32_e32 v87, v2
	v_mov_b32_e32 v88, v2
	v_mov_b32_e32 v89, v2
	v_mov_b32_e32 v98, v2
	v_mov_b32_e32 v99, v2
	v_mov_b32_e32 v100, v2
	v_mov_b32_e32 v101, v2
	v_mov_b32_e32 v102, v2
	v_mov_b32_e32 v103, v2
	v_mov_b32_e32 v104, v2
	v_mov_b32_e32 v105, v2
	v_mov_b32_e32 v114, v2
	v_mov_b32_e32 v115, v2
	v_mov_b32_e32 v116, v2
	v_mov_b32_e32 v117, v2
	v_mov_b32_e32 v134, v2
	v_mov_b32_e32 v135, v2
	v_mov_b32_e32 v136, v2
	v_mov_b32_e32 v137, v2
	v_mov_b32_e32 v74, v2
	v_mov_b32_e32 v75, v2
	v_mov_b32_e32 v76, v2
	v_mov_b32_e32 v77, v2
	v_mov_b32_e32 v78, v2
	v_mov_b32_e32 v79, v2
	v_mov_b32_e32 v80, v2
	v_mov_b32_e32 v81, v2
	v_mov_b32_e32 v90, v2
	v_mov_b32_e32 v91, v2
	v_mov_b32_e32 v92, v2
	v_mov_b32_e32 v93, v2
	v_mov_b32_e32 v94, v2
	v_mov_b32_e32 v95, v2
	v_mov_b32_e32 v96, v2
	v_mov_b32_e32 v97, v2
	v_mov_b32_e32 v106, v2
	v_mov_b32_e32 v107, v2
	v_mov_b32_e32 v108, v2
	v_mov_b32_e32 v109, v2
	v_mov_b32_e32 v110, v2
	v_mov_b32_e32 v111, v2
	v_mov_b32_e32 v112, v2
	v_mov_b32_e32 v113, v2
	v_mov_b32_e32 v138, v2
	v_mov_b32_e32 v139, v2
	v_mov_b32_e32 v140, v2
	v_mov_b32_e32 v141, v2
	v_mov_b32_e32 v142, v2
	v_mov_b32_e32 v143, v2
	v_mov_b32_e32 v144, v2
	v_mov_b32_e32 v145, v2
	s_branch .LBB0_683
	s_nop 0
	s_nop 0
	s_nop 0
	s_nop 0
	s_nop 0
	s_nop 0

; #define PG8_STAGE(bufoff, gbase, voff) do { _Pragma("unroll") for (int _i = 0; _i < 2; ++_i) \
;         __builtin_amdgcn_global_load_lds((const unsigned*)((const char*)(gbase) + (voff)[_i]), (LAS unsigned*)(lds + (bufoff) + ldsw + _i * 8192), 16, 0, 0); } while (0)
; #define PG8_WAIT_V(n) asm volatile("s_waitcnt vmcnt(" #n ")" ::: "memory")
; #define PG8_BAR __builtin_amdgcn_s_barrier()
;     ...
;     Unit cur, nxt; int ui = 0;
;     if (!S.next(0, cur)) return;
;     f32x4 acc[2][2][4][2];
; #pragma unroll
;     for (int a = 0; a < 2; ++a)
; #pragma unroll
;         for (int b = 0; b < 2; ++b)
; #pragma unroll
;             for (int m = 0; m < 4; ++m)
; #pragma unroll
;                 for (int n = 0; n < 2; ++n) acc[a][b][m][n] = (f32x4){0.f, 0.f, 0.f, 0.f};
;     bf16x8 At[4][2], B0[2][2], B1[2][2];
;     unsigned va[2][2], vn[2][2];
;     PG8_ROWS(va, cur);
;     const char* cA = (const char*)A; const char* cB = S.b_base(cur);
;     PG8_WAIT_V(0);
;     PG8_STAGE(PG8_SB(0, 0), cB, voffB); PG8_STAGE(PG8_SB(0, 1), cB + hstep, voffB); PG8_STAGE(PG8_SA(0, 0), cA, va[0]); PG8_STAGE(PG8_SA(0, 1), cA, va[1]);
;     if (wr == 1) PG8_BAR;
;     PG8_WAIT_V(2); PG8_BAR;
;     PG8_STAGE(PG8_SB(1, 0), cB + kstep, voffB); PG8_STAGE(PG8_SA(1, 0), cA + kstep, va[0]); PG8_STAGE(PG8_SB(1, 1), cB + hstep + kstep, voffB);
;     PG8_WAIT_V(6); PG8_BAR;
;     for (;;) {
;         const bool has_next = S.next(ui + 1, nxt);
;         if (has_next) { PG8_ROWS(vn, nxt); }
;         else {
; #pragma unroll
;             for (int h = 0; h < 2; ++h)
; #pragma unroll
;                 for (int i = 0; i < 2; ++i) vn[h][i] = va[h][i]; }
;         const char* nB = has_next ? S.b_base(nxt) : cB;
;         for (int t = 0; t < nt; t += 2) {
;             const bool last = (t == nt - 2);
;             const char* a1 = cA + (size_t)(t + 1) * kstep;
;             const char* a2 = last ? cA : cA + (size_t)(t + 2) * kstep; const char* b2 = last ? nB : cB + (size_t)(t + 2) * kstep;
;             const char* a3 = a2 + kstep; const char* b3 = b2 + kstep;
;     ...
; #pragma unroll
;         for (int a = 0; a < 2; ++a)
; #pragma unroll
;             for (int b = 0; b < 2; ++b)
; #pragma unroll
;                 for (int m = 0; m < 4; ++m)
; #pragma unroll
;                     for (int n = 0; n < 2; ++n) acc[a][b][m][n] = (f32x4){0.f, 0.f, 0.f, 0.f};
;         cur = nxt; cB = nB; ++ui;
.LBB0_1033:
	s_add_u32 s43, s48, 0x100
	v_mov_b32_e32 v66, 0
	v_mov_b32_e32 v209, v201
	v_mov_b32_e32 v211, v201
	s_addc_u32 s45, s49, 0
	s_mov_b32 s70, -2
	s_mov_b64 s[48:49], s[28:29]
	v_mov_b32_e32 v67, v66
	v_mov_b32_e32 v68, v66
	v_mov_b32_e32 v69, v66
	v_mov_b32_e32 v74, v66
	v_mov_b32_e32 v75, v66
	v_mov_b32_e32 v76, v66
	v_mov_b32_e32 v77, v66
	v_mov_b32_e32 v82, v66
	v_mov_b32_e32 v83, v66
	v_mov_b32_e32 v84, v66
	v_mov_b32_e32 v85, v66
	v_mov_b32_e32 v90, v66
	v_mov_b32_e32 v91, v66
	v_mov_b32_e32 v92, v66
	v_mov_b32_e32 v93, v66
	v_mov_b32_e32 v98, v66
	v_mov_b32_e32 v99, v66
	v_mov_b32_e32 v100, v66
	v_mov_b32_e32 v101, v66
	v_mov_b32_e32 v106, v66
	v_mov_b32_e32 v107, v66
	v_mov_b32_e32 v108, v66
	v_mov_b32_e32 v109, v66
	v_mov_b32_e32 v114, v66
	v_mov_b32_e32 v115, v66
	v_mov_b32_e32 v116, v66
	v_mov_b32_e32 v117, v66
	v_mov_b32_e32 v122, v66
	v_mov_b32_e32 v123, v66
	v_mov_b32_e32 v124, v66
	v_mov_b32_e32 v125, v66
	v_mov_b32_e32 v70, v66
	v_mov_b32_e32 v71, v66
	v_mov_b32_e32 v72, v66
	v_mov_b32_e32 v73, v66
	v_mov_b32_e32 v78, v66
	v_mov_b32_e32 v79, v66
	v_mov_b32_e32 v80, v66
	v_mov_b32_e32 v81, v66
	v_mov_b32_e32 v86, v66
	v_mov_b32_e32 v87, v66
	v_mov_b32_e32 v88, v66
	v_mov_b32_e32 v89, v66
	v_mov_b32_e32 v94, v66
	v_mov_b32_e32 v95, v66
	v_mov_b32_e32 v96, v66
	v_mov_b32_e32 v97, v66
	v_mov_b32_e32 v102, v66
	v_mov_b32_e32 v103, v66
	v_mov_b32_e32 v104, v66
	v_mov_b32_e32 v105, v66
	v_mov_b32_e32 v110, v66
	v_mov_b32_e32 v111, v66
	v_mov_b32_e32 v112, v66
	v_mov_b32_e32 v113, v66
	v_mov_b32_e32 v118, v66
	v_mov_b32_e32 v119, v66
	v_mov_b32_e32 v120, v66
	v_mov_b32_e32 v121, v66
	v_mov_b32_e32 v126, v66
	v_mov_b32_e32 v127, v66
	v_mov_b32_e32 v128, v66
	v_mov_b32_e32 v129, v66
	v_mov_b32_e32 v130, v66
	v_mov_b32_e32 v131, v66
	v_mov_b32_e32 v132, v66
	v_mov_b32_e32 v133, v66
	v_mov_b32_e32 v138, v66
	v_mov_b32_e32 v139, v66
	v_mov_b32_e32 v140, v66
	v_mov_b32_e32 v141, v66
	v_mov_b32_e32 v146, v66
	v_mov_b32_e32 v147, v66
	v_mov_b32_e32 v148, v66
	v_mov_b32_e32 v149, v66
	v_mov_b32_e32 v154, v66
	v_mov_b32_e32 v155, v66
	v_mov_b32_e32 v156, v66
	v_mov_b32_e32 v157, v66
	v_mov_b32_e32 v162, v66
	v_mov_b32_e32 v163, v66
	v_mov_b32_e32 v164, v66
	v_mov_b32_e32 v165, v66
	v_mov_b32_e32 v170, v66
	v_mov_b32_e32 v171, v66
	v_mov_b32_e32 v172, v66
	v_mov_b32_e32 v173, v66
	v_mov_b32_e32 v178, v66
	v_mov_b32_e32 v179, v66
	v_mov_b32_e32 v180, v66
	v_mov_b32_e32 v181, v66
	v_mov_b32_e32 v186, v66
	v_mov_b32_e32 v187, v66
	v_mov_b32_e32 v188, v66
	v_mov_b32_e32 v189, v66
	v_mov_b32_e32 v134, v66
	v_mov_b32_e32 v135, v66
	v_mov_b32_e32 v136, v66
	v_mov_b32_e32 v137, v66
	v_mov_b32_e32 v142, v66
	v_mov_b32_e32 v143, v66
	v_mov_b32_e32 v144, v66
	v_mov_b32_e32 v145, v66
	v_mov_b32_e32 v150, v66
	v_mov_b32_e32 v151, v66
	v_mov_b32_e32 v152, v66
	v_mov_b32_e32 v153, v66
	v_mov_b32_e32 v158, v66
	v_mov_b32_e32 v159, v66
	v_mov_b32_e32 v160, v66
	v_mov_b32_e32 v161, v66
	v_mov_b32_e32 v166, v66
	v_mov_b32_e32 v167, v66
	v_mov_b32_e32 v168, v66
	v_mov_b32_e32 v169, v66
	v_mov_b32_e32 v174, v66
	v_mov_b32_e32 v175, v66
	v_mov_b32_e32 v176, v66
	v_mov_b32_e32 v177, v66
	v_mov_b32_e32 v182, v66
	v_mov_b32_e32 v183, v66
	v_mov_b32_e32 v184, v66
	v_mov_b32_e32 v185, v66
	v_mov_b32_e32 v190, v66
	v_mov_b32_e32 v191, v66
	v_mov_b32_e32 v192, v66
	v_mov_b32_e32 v193, v66
	s_branch .LBB0_1036
	s_nop 0
	s_nop 0
	s_nop 0
	s_nop 0
	s_nop 0
	s_nop 0
	s_nop 0
	s_nop 0
	s_nop 0
	s_nop 0
	s_nop 0
	s_nop 0
	s_nop 0
	s_nop 0
	s_nop 0

; #define PG8_STAGE(bufoff, gbase, voff) do { _Pragma("unroll") for (int _i = 0; _i < 2; ++_i) \
;         __builtin_amdgcn_global_load_lds((const unsigned*)((const char*)(gbase) + (voff)[_i]), (LAS unsigned*)(lds + (bufoff) + ldsw + _i * 8192), 16, 0, 0); } while (0)
; #define PG8_WAIT_V(n) asm volatile("s_waitcnt vmcnt(" #n ")" ::: "memory")
; #define PG8_BAR __builtin_amdgcn_s_barrier()
;     ...
;     Unit cur, nxt; int ui = 0;
;     if (!S.next(0, cur)) return;
;     f32x4 acc[2][2][4][2];
; #pragma unroll
;     for (int a = 0; a < 2; ++a)
; #pragma unroll
;         for (int b = 0; b < 2; ++b)
; #pragma unroll
;             for (int m = 0; m < 4; ++m)
; #pragma unroll
;                 for (int n = 0; n < 2; ++n) acc[a][b][m][n] = (f32x4){0.f, 0.f, 0.f, 0.f};
;     bf16x8 At[4][2], B0[2][2], B1[2][2];
;     unsigned va[2][2], vn[2][2];
;     PG8_ROWS(va, cur);
;     const char* cA = (const char*)A; const char* cB = S.b_base(cur);
;     PG8_WAIT_V(0);
;     PG8_STAGE(PG8_SB(0, 0), cB, voffB); PG8_STAGE(PG8_SB(0, 1), cB + hstep, voffB); PG8_STAGE(PG8_SA(0, 0), cA, va[0]); PG8_STAGE(PG8_SA(0, 1), cA, va[1]);
;     if (wr == 1) PG8_BAR;
;     PG8_WAIT_V(2); PG8_BAR;
;     PG8_STAGE(PG8_SB(1, 0), cB + kstep, voffB); PG8_STAGE(PG8_SA(1, 0), cA + kstep, va[0]); PG8_STAGE(PG8_SB(1, 1), cB + hstep + kstep, voffB);
;     PG8_WAIT_V(6); PG8_BAR;
;     for (;;) {
;         const bool has_next = S.next(ui + 1, nxt);
;         if (has_next) { PG8_ROWS(vn, nxt); }
;         else {
; #pragma unroll
;             for (int h = 0; h < 2; ++h)
; #pragma unroll
;                 for (int i = 0; i < 2; ++i) vn[h][i] = va[h][i]; }
;         const char* nB = has_next ? S.b_base(nxt) : cB;
;         for (int t = 0; t < nt; t += 2) {
;             const bool last = (t == nt - 2);
;             const char* a1 = cA + (size_t)(t + 1) * kstep;
;             const char* a2 = last ? cA : cA + (size_t)(t + 2) * kstep; const char* b2 = last ? nB : cB + (size_t)(t + 2) * kstep;
;             const char* a3 = a2 + kstep; const char* b3 = b2 + kstep;
;     ...
; #pragma unroll
;         for (int a = 0; a < 2; ++a)
; #pragma unroll
;             for (int b = 0; b < 2; ++b)
; #pragma unroll
;                 for (int m = 0; m < 4; ++m)
; #pragma unroll
;                     for (int n = 0; n < 2; ++n) acc[a][b][m][n] = (f32x4){0.f, 0.f, 0.f, 0.f};
;         cur = nxt; cB = nB; ++ui;
.LBB0_1185:
	s_add_u32 s27, s34, 0x100
	v_mov_b32_e32 v66, 0
	v_mov_b32_e32 v209, v201
	v_mov_b32_e32 v211, v201
	s_addc_u32 s29, s35, 0
	s_mov_b32 s62, -2
	s_mov_b64 s[34:35], s[12:13]
	v_mov_b32_e32 v67, v66
	v_mov_b32_e32 v68, v66
	v_mov_b32_e32 v69, v66
	v_mov_b32_e32 v70, v66
	v_mov_b32_e32 v71, v66
	v_mov_b32_e32 v72, v66
	v_mov_b32_e32 v73, v66
	v_mov_b32_e32 v74, v66
	v_mov_b32_e32 v75, v66
	v_mov_b32_e32 v76, v66
	v_mov_b32_e32 v77, v66
	v_mov_b32_e32 v78, v66
	v_mov_b32_e32 v79, v66
	v_mov_b32_e32 v80, v66
	v_mov_b32_e32 v81, v66
	v_mov_b32_e32 v98, v66
	v_mov_b32_e32 v99, v66
	v_mov_b32_e32 v100, v66
	v_mov_b32_e32 v101, v66
	v_mov_b32_e32 v102, v66
	v_mov_b32_e32 v103, v66
	v_mov_b32_e32 v104, v66
	v_mov_b32_e32 v105, v66
	v_mov_b32_e32 v106, v66
	v_mov_b32_e32 v107, v66
	v_mov_b32_e32 v108, v66
	v_mov_b32_e32 v109, v66
	v_mov_b32_e32 v110, v66
	v_mov_b32_e32 v111, v66
	v_mov_b32_e32 v112, v66
	v_mov_b32_e32 v113, v66
	v_mov_b32_e32 v82, v66
	v_mov_b32_e32 v83, v66
	v_mov_b32_e32 v84, v66
	v_mov_b32_e32 v85, v66
	v_mov_b32_e32 v86, v66
	v_mov_b32_e32 v87, v66
	v_mov_b32_e32 v88, v66
	v_mov_b32_e32 v89, v66
	v_mov_b32_e32 v90, v66
	v_mov_b32_e32 v91, v66
	v_mov_b32_e32 v92, v66
	v_mov_b32_e32 v93, v66
	v_mov_b32_e32 v94, v66
	v_mov_b32_e32 v95, v66
	v_mov_b32_e32 v96, v66
	v_mov_b32_e32 v97, v66
	v_mov_b32_e32 v114, v66
	v_mov_b32_e32 v115, v66
	v_mov_b32_e32 v116, v66
	v_mov_b32_e32 v117, v66
	v_mov_b32_e32 v118, v66
	v_mov_b32_e32 v119, v66
	v_mov_b32_e32 v120, v66
	v_mov_b32_e32 v121, v66
	v_mov_b32_e32 v122, v66
	v_mov_b32_e32 v123, v66
	v_mov_b32_e32 v124, v66
	v_mov_b32_e32 v125, v66
	v_mov_b32_e32 v126, v66
	v_mov_b32_e32 v127, v66
	v_mov_b32_e32 v128, v66
	v_mov_b32_e32 v129, v66
	v_mov_b32_e32 v130, v66
	v_mov_b32_e32 v131, v66
	v_mov_b32_e32 v132, v66
	v_mov_b32_e32 v133, v66
	v_mov_b32_e32 v134, v66
	v_mov_b32_e32 v135, v66
	v_mov_b32_e32 v136, v66
	v_mov_b32_e32 v137, v66
	v_mov_b32_e32 v138, v66
	v_mov_b32_e32 v139, v66
	v_mov_b32_e32 v140, v66
	v_mov_b32_e32 v141, v66
	v_mov_b32_e32 v142, v66
	v_mov_b32_e32 v143, v66
	v_mov_b32_e32 v144, v66
	v_mov_b32_e32 v145, v66
	v_mov_b32_e32 v162, v66
	v_mov_b32_e32 v163, v66
	v_mov_b32_e32 v164, v66
	v_mov_b32_e32 v165, v66
	v_mov_b32_e32 v166, v66
	v_mov_b32_e32 v167, v66
	v_mov_b32_e32 v168, v66
	v_mov_b32_e32 v169, v66
	v_mov_b32_e32 v170, v66
	v_mov_b32_e32 v171, v66
	v_mov_b32_e32 v172, v66
	v_mov_b32_e32 v173, v66
	v_mov_b32_e32 v174, v66
	v_mov_b32_e32 v175, v66
	v_mov_b32_e32 v176, v66
	v_mov_b32_e32 v177, v66
	v_mov_b32_e32 v146, v66
	v_mov_b32_e32 v147, v66
	v_mov_b32_e32 v148, v66
	v_mov_b32_e32 v149, v66
	v_mov_b32_e32 v150, v66
	v_mov_b32_e32 v151, v66
	v_mov_b32_e32 v152, v66
	v_mov_b32_e32 v153, v66
	v_mov_b32_e32 v154, v66
	v_mov_b32_e32 v155, v66
	v_mov_b32_e32 v156, v66
	v_mov_b32_e32 v157, v66
	v_mov_b32_e32 v158, v66
	v_mov_b32_e32 v159, v66
	v_mov_b32_e32 v160, v66
	v_mov_b32_e32 v161, v66
	v_mov_b32_e32 v178, v66
	v_mov_b32_e32 v179, v66
	v_mov_b32_e32 v180, v66
	v_mov_b32_e32 v181, v66
	v_mov_b32_e32 v182, v66
	v_mov_b32_e32 v183, v66
	v_mov_b32_e32 v184, v66
	v_mov_b32_e32 v185, v66
	v_mov_b32_e32 v186, v66
	v_mov_b32_e32 v187, v66
	v_mov_b32_e32 v188, v66
	v_mov_b32_e32 v189, v66
	v_mov_b32_e32 v190, v66
	v_mov_b32_e32 v191, v66
	v_mov_b32_e32 v192, v66
	v_mov_b32_e32 v193, v66
	s_branch .LBB0_1188
	s_nop 0
	s_nop 0
	s_nop 0
